# v39 + anti-phased sectional priority in the MLA steady loops: s_setprio 1 while a wave is in its PV section, 0 in its QK section
# baseline (speedup 1.0000x reference)
; template <bool FOX>
; __device__ __forceinline__ void attn_unit(const Args& A, int b, int h, int qb, LAS char* shm, LAS float* dg) {
;     ...
;     for (int t = 1; t < t_end; ++t) {
;         if (t == 1 && 4 < nti) ISSUE_K(t0 + 4, 0);
;         if (t + 4 < nti) ISSUE_K(t0 + t + 4, t % NS);
;         if (t + 2 < nti) ISSUE_V(t0 + t + 2, (t + 2) % NS);
;         SFENCE();
;         { if constexpr (!FOX) { if (t0 + t == tw_last + 1) {
; #pragma unroll
;                   for (int r = 0; r < 16; ++r) negm[r] = -INFINITY;
;                   asm volatile("" : "+v"(negm)); } }
;           const lds_cptr vp = vp0 + ((t - 1) % NS) * VSLOT; float sa = 0.f, sb = 0.f;
; #pragma unroll
;           for (int g = 0; g < 2 * NQ; ++g) {
;               if (!FOX && g == 0) c0 = __builtin_amdgcn_mfma_f32_32x32x16_bf16(kf[0], qr[0], negm, 0, 0, 0);
;               else if (!FOX && g == 1) c1 = __builtin_amdgcn_mfma_f32_32x32x16_bf16(kf[1], qr[0], negm, 0, 0, 0);
;               else if (g & 1) c1 = __builtin_amdgcn_mfma_f32_32x32x16_bf16(kf[g], qr[g >> 1], c1, 0, 0, 0); else c0 = __builtin_amdgcn_mfma_f32_32x32x16_bf16(kf[g], qr[g >> 1], c0, 0, 0, 0);
;               if (g < 8) { const int i = (g >> 1) + 4 * (g & 1); vlo[i] = vtr(vp + (i >> 2) * 4096 + (i & 3) * 1024); vhi[i] = vtr(vp + (i >> 2) * 4096 + (i & 3) * 1024 + 512);
;                   if (g < 4) { sa += pp0[4 * g]; sb += pp0[4 * g + 1]; sa += pp0[4 * g + 2]; sb += pp0[4 * g + 3]; } else { sa += pp1[4 * g - 16]; sb += pp1[4 * g - 15]; sa += pp1[4 * g - 14]; sb += pp1[4 * g - 13]; }
;                   asm volatile("" : "+v"(sa), "+v"(sb)); }
;               { constexpr int G0 = FOX ? 0 : 4; if (g >= G0) { const int q = 2 * (g - G0);
; #pragma unroll
;                   for (int k = 0; k < 2; ++k) { const int w = q + k; const unsigned pkd = w < 8 ? cvt_pk_bf16(pp0[2 * w], pp0[2 * w + 1]) : cvt_pk_bf16(pp1[2 * w - 16], pp1[2 * w - 15]); pw[w >> 2][w & 3] = pkd; } } }
;               SFENCE();
;           }
;           lrun += sa + sb; }
;         MASKONLY(t);
;         float rm; ROWMAX(rm);
;         bool resc = false;
;         if (__any(rm > THR)) { const float dl = fmaxf(rm, 0.f); mhat += dl;
; #pragma unroll
;             for (int r = 0; r < 16; ++r) { c0[r] -= dl; c1[r] -= dl; }
;             if constexpr (!FOX) {
; #pragma unroll
;                 for (int r = 0; r < 16; ++r) negm[r] = -mhat;
.Lmla_ss1_in:
	s_mov_b32 m0, s52
	s_nop 0
	global_load_lds_dwordx4 v240, s[46:47]
	s_add_i32 m0, s52, 0x2000
	s_nop 0
	global_load_lds_dwordx4 v240, s[98:99]
	s_mov_b32 m0, s53
	s_nop 0
	global_load_lds_dwordx4 v240, s[60:61]
	s_waitcnt lgkmcnt(0)
	s_setprio 0
	s_add_i32 s27, s42, 0x8000
	v_mfma_f32_32x32x16_bf16 v[114:129], v[206:209], v[138:141], v[82:97]
	s_and_b32 s27, s27, 0x6000
	s_add_u32 s42, s42, 0x2000
	s_addc_u32 s43, s43, 0
	v_add_u32_e32 v3, s27, v247
	ds_read_b64_tr_b16 v[206:207], v3 offset:49152
	ds_read_b64_tr_b16 v[208:209], v3 offset:49664
	v_add_f32_e32 v4, v69, v67
	v_add_f32_e32 v5, v68, v66
	v_mfma_f32_32x32x16_bf16 v[98:113], v[194:197], v[138:141], v[82:97]
	ds_read_b64_tr_b16 v[194:195], v3 offset:53248
	ds_read_b64_tr_b16 v[196:197], v3 offset:53760
	v_add_f32_e32 v4, v71, v4
	v_add_f32_e32 v5, v70, v5
	v_add_f32_e32 v4, v73, v4
	v_add_f32_e32 v5, v72, v5
	v_mfma_f32_32x32x16_bf16 v[114:129], v[202:205], v[142:145], v[114:129]
	ds_read_b64_tr_b16 v[202:203], v3 offset:50176
	ds_read_b64_tr_b16 v[204:205], v3 offset:50688
	v_add_f32_e32 v4, v75, v4
	v_add_f32_e32 v5, v74, v5
	v_add_f32_e32 v4, v77, v4
	v_add_f32_e32 v5, v76, v5
	v_mfma_f32_32x32x16_bf16 v[98:113], v[186:189], v[142:145], v[98:113]
	ds_read_b64_tr_b16 v[214:215], v3 offset:54272
	ds_read_b64_tr_b16 v[216:217], v3 offset:54784
	v_add_f32_e32 v4, v79, v4
	v_add_f32_e32 v5, v78, v5
	v_add_f32_e32 v4, v81, v4
	v_add_f32_e32 v5, v80, v5
	v_mfma_f32_32x32x16_bf16 v[114:129], v[198:201], v[146:149], v[114:129]
	ds_read_b64_tr_b16 v[210:211], v3 offset:51200
	ds_read_b64_tr_b16 v[212:213], v3 offset:51712
	v_add_f32_e32 v4, v51, v4
	v_add_f32_e32 v5, v50, v5
	v_add_f32_e32 v4, v53, v4
	v_add_f32_e32 v5, v52, v5
	v_mfma_f32_32x32x16_bf16 v[98:113], v[182:185], v[146:149], v[98:113]
	ds_read_b64_tr_b16 v[12:13], v3 offset:55296
	ds_read_b64_tr_b16 v[14:15], v3 offset:55808
	v_add_f32_e32 v4, v55, v4
	v_add_f32_e32 v5, v54, v5
	v_add_f32_e32 v4, v57, v4
	v_add_f32_e32 v5, v56, v5
	v_mfma_f32_32x32x16_bf16 v[114:129], v[190:193], v[150:153], v[114:129]
	ds_read_b64_tr_b16 v[8:9], v3 offset:52224
	ds_read_b64_tr_b16 v[10:11], v3 offset:52736
	v_add_f32_e32 v4, v59, v4
	v_add_f32_e32 v16, v61, v4
	v_add_f32_e32 v4, v58, v5
	v_add_f32_e32 v17, v60, v4
	v_mfma_f32_32x32x16_bf16 v[98:113], v[170:173], v[150:153], v[98:113]
	s_add_u32 s46, s46, s62
	s_addc_u32 s47, s47, s63
	s_and_b32 s64, s26, 3
	ds_read_b64_tr_b16 v[4:5], v3 offset:56320
	ds_read_b64_tr_b16 v[6:7], v3 offset:56832
	v_add_f32_e32 v3, v63, v16
	v_add_f32_e32 v16, v62, v17
	v_add_f32_e32 v3, v65, v3
	v_add_f32_e32 v16, v64, v16
	v_mfma_f32_32x32x16_bf16 v[114:129], v[178:181], v[154:157], v[114:129]
	s_mulk_i32 s64, 0x3000
	s_add_u32 s60, s60, 0x2000
	s_addc_u32 s61, s61, 0
	v_cvt_pk_bf16_f32 v178, v50, v51
	v_cvt_pk_bf16_f32 v179, v52, v53
	v_cvt_pk_bf16_f32 v186, v66, v67
	v_cvt_pk_bf16_f32 v187, v68, v69
	v_mfma_f32_32x32x16_bf16 v[98:113], v[166:169], v[154:157], v[98:113]
	s_add_i32 s52, s64, s91
	s_add_i32 s64, s42, 0x6000
	s_add_u32 s98, s98, s62
	s_addc_u32 s99, s99, s63
	v_cvt_pk_bf16_f32 v180, v54, v55
	v_cvt_pk_bf16_f32 v181, v56, v57
	v_cvt_pk_bf16_f32 v188, v70, v71
	v_cvt_pk_bf16_f32 v189, v72, v73
	v_mfma_f32_32x32x16_bf16 v[114:129], v[174:177], v[158:161], v[114:129]
	s_and_b32 s64, s64, 0x6000
	s_add_i32 s53, s64, s93
	v_cvt_pk_bf16_f32 v218, v58, v59
	v_cvt_pk_bf16_f32 v219, v60, v61
	v_cvt_pk_bf16_f32 v182, v74, v75
	v_cvt_pk_bf16_f32 v183, v76, v77
	v_mfma_f32_32x32x16_bf16 v[98:113], v[162:165], v[158:161], v[98:113]
	v_cvt_pk_bf16_f32 v220, v62, v63
	v_cvt_pk_bf16_f32 v221, v64, v65
	v_cvt_pk_bf16_f32 v184, v78, v79
	v_cvt_pk_bf16_f32 v185, v80, v81
	v_add_f32_e32 v3, v3, v16
	v_add_f32_e32 v246, v246, v3
	s_nop 3
	s_waitcnt lgkmcnt(0)
	s_setprio 1
	v_mfma_f32_32x32x16_bf16 v[18:33], v[186:189], v[206:209], v[18:33]
	s_add_i32 s27, s26, 1
	s_and_b32 s64, s27, 3
	s_mulk_i32 s64, 0x3000
	v_exp_f32_e32 v66, v114
	v_exp_f32_e32 v67, v115
	v_exp_f32_e32 v68, v116
	v_exp_f32_e32 v69, v117
	v_add_u32_e32 v3, s64, v248
	v_mfma_f32_32x32x16_bf16 v[34:49], v[186:189], v[194:197], v[34:49]
	v_exp_f32_e32 v70, v118
	v_exp_f32_e32 v71, v119
	v_exp_f32_e32 v72, v120
	v_exp_f32_e32 v73, v121
	ds_read_b128 v[206:209], v3
	ds_read_b128 v[194:197], v3 offset:512
	v_mfma_f32_32x32x16_bf16 v[18:33], v[182:185], v[202:205], v[18:33]
	v_exp_f32_e32 v74, v122
	v_exp_f32_e32 v75, v123
	v_exp_f32_e32 v76, v124
	v_exp_f32_e32 v77, v125
	ds_read_b128 v[202:205], v3 offset:2048
	ds_read_b128 v[186:189], v3 offset:2560
	v_mfma_f32_32x32x16_bf16 v[34:49], v[182:185], v[214:217], v[34:49]
	v_exp_f32_e32 v78, v126
	v_exp_f32_e32 v79, v127
	v_exp_f32_e32 v80, v128
	v_exp_f32_e32 v81, v129
	ds_read_b128 v[198:201], v3 offset:4096
	ds_read_b128 v[182:185], v3 offset:4608
	v_mfma_f32_32x32x16_bf16 v[18:33], v[178:181], v[210:213], v[18:33]
	v_exp_f32_e32 v50, v98
	v_exp_f32_e32 v51, v99
	v_exp_f32_e32 v52, v100
	v_exp_f32_e32 v53, v101
	ds_read_b128 v[190:193], v3 offset:6144
	ds_read_b128 v[170:173], v3 offset:6656
	v_mfma_f32_32x32x16_bf16 v[34:49], v[178:181], v[12:15], v[34:49]
	v_exp_f32_e32 v54, v102
	v_exp_f32_e32 v55, v103
	v_exp_f32_e32 v56, v104
	v_exp_f32_e32 v57, v105
	ds_read_b128 v[178:181], v3 offset:8192
	ds_read_b128 v[166:169], v3 offset:8704
	v_mfma_f32_32x32x16_bf16 v[18:33], v[218:221], v[8:11], v[18:33]
	v_exp_f32_e32 v58, v106
	v_exp_f32_e32 v59, v107
	v_exp_f32_e32 v60, v108
	v_exp_f32_e32 v61, v109
	ds_read_b128 v[174:177], v3 offset:10240
	ds_read_b128 v[162:165], v3 offset:10752
	v_mfma_f32_32x32x16_bf16 v[34:49], v[218:221], v[4:7], v[34:49]
	v_exp_f32_e32 v62, v110
	v_exp_f32_e32 v63, v111
	v_exp_f32_e32 v64, v112
	v_exp_f32_e32 v65, v113
	s_mov_b32 s26, s27
	s_cmp_eq_u32 s27, s96
	s_cbranch_scc1 .Lmla_ss1_xdone
	s_add_i32 s64, s27, 3
	s_cmp_lt_u32 s64, s94
	s_cbranch_scc1 .Lmla_ss1_top
	s_waitcnt vmcnt(4)
	s_barrier
	s_branch .Lmla_ss_back

; template <bool FOX>
; __device__ __forceinline__ void attn_unit(const Args& A, int b, int h, int qb, LAS char* shm, LAS float* dg) {
;     ...
;     for (int t = 1; t < t_end; ++t) {
;         if (t == 1 && 4 < nti) ISSUE_K(t0 + 4, 0);
;         if (t + 4 < nti) ISSUE_K(t0 + t + 4, t % NS);
;         if (t + 2 < nti) ISSUE_V(t0 + t + 2, (t + 2) % NS);
;         SFENCE();
;         { if constexpr (!FOX) { if (t0 + t == tw_last + 1) {
; #pragma unroll
;                   for (int r = 0; r < 16; ++r) negm[r] = -INFINITY;
;                   asm volatile("" : "+v"(negm)); } }
;           const lds_cptr vp = vp0 + ((t - 1) % NS) * VSLOT; float sa = 0.f, sb = 0.f;
; #pragma unroll
;           for (int g = 0; g < 2 * NQ; ++g) {
;               if (!FOX && g == 0) c0 = __builtin_amdgcn_mfma_f32_32x32x16_bf16(kf[0], qr[0], negm, 0, 0, 0);
;               else if (!FOX && g == 1) c1 = __builtin_amdgcn_mfma_f32_32x32x16_bf16(kf[1], qr[0], negm, 0, 0, 0);
;               else if (g & 1) c1 = __builtin_amdgcn_mfma_f32_32x32x16_bf16(kf[g], qr[g >> 1], c1, 0, 0, 0); else c0 = __builtin_amdgcn_mfma_f32_32x32x16_bf16(kf[g], qr[g >> 1], c0, 0, 0, 0);
;               if (g < 8) { const int i = (g >> 1) + 4 * (g & 1); vlo[i] = vtr(vp + (i >> 2) * 4096 + (i & 3) * 1024); vhi[i] = vtr(vp + (i >> 2) * 4096 + (i & 3) * 1024 + 512);
;                   if (g < 4) { sa += pp0[4 * g]; sb += pp0[4 * g + 1]; sa += pp0[4 * g + 2]; sb += pp0[4 * g + 3]; } else { sa += pp1[4 * g - 16]; sb += pp1[4 * g - 15]; sa += pp1[4 * g - 14]; sb += pp1[4 * g - 13]; }
;                   asm volatile("" : "+v"(sa), "+v"(sb)); }
;               { constexpr int G0 = FOX ? 0 : 4; if (g >= G0) { const int q = 2 * (g - G0);
; #pragma unroll
;                   for (int k = 0; k < 2; ++k) { const int w = q + k; const unsigned pkd = w < 8 ? cvt_pk_bf16(pp0[2 * w], pp0[2 * w + 1]) : cvt_pk_bf16(pp1[2 * w - 16], pp1[2 * w - 15]); pw[w >> 2][w & 3] = pkd; } } }
;               SFENCE();
;           }
;           lrun += sa + sb; }
;         MASKONLY(t);
;         float rm; ROWMAX(rm);
;         bool resc = false;
;         if (__any(rm > THR)) { const float dl = fmaxf(rm, 0.f); mhat += dl;
; #pragma unroll
;             for (int r = 0; r < 16; ++r) { c0[r] -= dl; c1[r] -= dl; }
;             if constexpr (!FOX) {
; #pragma unroll
;                 for (int r = 0; r < 16; ++r) negm[r] = -mhat;
.Lmla_ss2_top:
	s_mov_b32 m0, s52
	s_nop 0
	global_load_lds_dwordx4 v240, s[46:47]
	s_mov_b32 m0, s53
	s_nop 0
	global_load_lds_dwordx4 v240, s[60:61]
	s_waitcnt lgkmcnt(0)
	s_setprio 0
	s_add_i32 s27, s42, 0x8000
	v_mfma_f32_32x32x16_bf16 v[114:129], v[206:209], v[138:141], v[82:97]
	s_and_b32 s27, s27, 0x6000
	s_add_u32 s42, s42, 0x2000
	s_addc_u32 s43, s43, 0
	v_add_u32_e32 v3, s27, v247
	ds_read_b64_tr_b16 v[206:207], v3 offset:49152
	ds_read_b64_tr_b16 v[208:209], v3 offset:49664
	v_add_f32_e32 v4, v69, v67
	v_add_f32_e32 v5, v68, v66
	v_mfma_f32_32x32x16_bf16 v[98:113], v[194:197], v[138:141], v[82:97]
	ds_read_b64_tr_b16 v[194:195], v3 offset:53248
	ds_read_b64_tr_b16 v[196:197], v3 offset:53760
	v_add_f32_e32 v4, v71, v4
	v_add_f32_e32 v5, v70, v5
	v_add_f32_e32 v4, v73, v4
	v_add_f32_e32 v5, v72, v5
	v_mfma_f32_32x32x16_bf16 v[114:129], v[202:205], v[142:145], v[114:129]
	ds_read_b64_tr_b16 v[202:203], v3 offset:50176
	ds_read_b64_tr_b16 v[204:205], v3 offset:50688
	v_add_f32_e32 v4, v75, v4
	v_add_f32_e32 v5, v74, v5
	v_add_f32_e32 v4, v77, v4
	v_add_f32_e32 v5, v76, v5
	v_mfma_f32_32x32x16_bf16 v[98:113], v[186:189], v[142:145], v[98:113]
	ds_read_b64_tr_b16 v[214:215], v3 offset:54272
	ds_read_b64_tr_b16 v[216:217], v3 offset:54784
	v_add_f32_e32 v4, v79, v4
	v_add_f32_e32 v5, v78, v5
	v_add_f32_e32 v4, v81, v4
	v_add_f32_e32 v5, v80, v5
	v_mfma_f32_32x32x16_bf16 v[114:129], v[198:201], v[146:149], v[114:129]
	ds_read_b64_tr_b16 v[210:211], v3 offset:51200
	ds_read_b64_tr_b16 v[212:213], v3 offset:51712
	v_add_f32_e32 v4, v51, v4
	v_add_f32_e32 v5, v50, v5
	v_add_f32_e32 v4, v53, v4
	v_add_f32_e32 v5, v52, v5
	v_mfma_f32_32x32x16_bf16 v[98:113], v[182:185], v[146:149], v[98:113]
	ds_read_b64_tr_b16 v[12:13], v3 offset:55296
	ds_read_b64_tr_b16 v[14:15], v3 offset:55808
	v_add_f32_e32 v4, v55, v4
	v_add_f32_e32 v5, v54, v5
	v_add_f32_e32 v4, v57, v4
	v_add_f32_e32 v5, v56, v5
	v_mfma_f32_32x32x16_bf16 v[114:129], v[190:193], v[150:153], v[114:129]
	ds_read_b64_tr_b16 v[8:9], v3 offset:52224
	ds_read_b64_tr_b16 v[10:11], v3 offset:52736
	v_add_f32_e32 v4, v59, v4
	v_add_f32_e32 v16, v61, v4
	v_add_f32_e32 v4, v58, v5
	v_add_f32_e32 v17, v60, v4
	v_mfma_f32_32x32x16_bf16 v[98:113], v[170:173], v[150:153], v[98:113]
	s_add_u32 s46, s46, s62
	s_addc_u32 s47, s47, s63
	s_and_b32 s64, s26, 3
	ds_read_b64_tr_b16 v[4:5], v3 offset:56320
	ds_read_b64_tr_b16 v[6:7], v3 offset:56832
	v_add_f32_e32 v3, v63, v16
	v_add_f32_e32 v16, v62, v17
	v_add_f32_e32 v3, v65, v3
	v_add_f32_e32 v16, v64, v16
	v_mfma_f32_32x32x16_bf16 v[114:129], v[178:181], v[154:157], v[114:129]
	s_mulk_i32 s64, 0x3000
	s_add_u32 s60, s60, 0x2000
	s_addc_u32 s61, s61, 0
	v_cvt_pk_bf16_f32 v178, v50, v51
	v_cvt_pk_bf16_f32 v179, v52, v53
	v_cvt_pk_bf16_f32 v186, v66, v67
	v_cvt_pk_bf16_f32 v187, v68, v69
	v_mfma_f32_32x32x16_bf16 v[98:113], v[166:169], v[154:157], v[98:113]
	s_add_i32 s52, s64, s91
	s_add_i32 s64, s42, 0x6000
	v_cvt_pk_bf16_f32 v180, v54, v55
	v_cvt_pk_bf16_f32 v181, v56, v57
	v_cvt_pk_bf16_f32 v188, v70, v71
	v_cvt_pk_bf16_f32 v189, v72, v73
	v_mfma_f32_32x32x16_bf16 v[114:129], v[174:177], v[158:161], v[114:129]
	s_and_b32 s64, s64, 0x6000
	s_add_i32 s53, s64, s93
	v_cvt_pk_bf16_f32 v218, v58, v59
	v_cvt_pk_bf16_f32 v219, v60, v61
	v_cvt_pk_bf16_f32 v182, v74, v75
	v_cvt_pk_bf16_f32 v183, v76, v77
	v_mfma_f32_32x32x16_bf16 v[98:113], v[162:165], v[158:161], v[98:113]
	v_cvt_pk_bf16_f32 v220, v62, v63
	v_cvt_pk_bf16_f32 v221, v64, v65
	v_cvt_pk_bf16_f32 v184, v78, v79
	v_cvt_pk_bf16_f32 v185, v80, v81
	v_add_f32_e32 v3, v3, v16
	v_add_f32_e32 v246, v246, v3
	s_waitcnt vmcnt(3)
	s_waitcnt lgkmcnt(0)
	s_barrier
	s_setprio 1
	v_mfma_f32_32x32x16_bf16 v[18:33], v[186:189], v[206:209], v[18:33]
	s_add_i32 s27, s26, 1
	s_and_b32 s64, s27, 3
	s_mulk_i32 s64, 0x3000
	v_exp_f32_e32 v66, v114
	v_exp_f32_e32 v67, v115
	v_exp_f32_e32 v68, v116
	v_exp_f32_e32 v69, v117
	v_add_u32_e32 v3, s64, v248
	v_mfma_f32_32x32x16_bf16 v[34:49], v[186:189], v[194:197], v[34:49]
	v_exp_f32_e32 v70, v118
	v_exp_f32_e32 v71, v119
	v_exp_f32_e32 v72, v120
	v_exp_f32_e32 v73, v121
	ds_read_b128 v[206:209], v3
	ds_read_b128 v[194:197], v3 offset:512
	v_mfma_f32_32x32x16_bf16 v[18:33], v[182:185], v[202:205], v[18:33]
	v_exp_f32_e32 v74, v122
	v_exp_f32_e32 v75, v123
	v_exp_f32_e32 v76, v124
	v_exp_f32_e32 v77, v125
	ds_read_b128 v[202:205], v3 offset:2048
	ds_read_b128 v[186:189], v3 offset:2560
	v_mfma_f32_32x32x16_bf16 v[34:49], v[182:185], v[214:217], v[34:49]
	v_exp_f32_e32 v78, v126
	v_exp_f32_e32 v79, v127
	v_exp_f32_e32 v80, v128
	v_exp_f32_e32 v81, v129
	ds_read_b128 v[198:201], v3 offset:4096
	ds_read_b128 v[182:185], v3 offset:4608
	v_mfma_f32_32x32x16_bf16 v[18:33], v[178:181], v[210:213], v[18:33]
	v_exp_f32_e32 v50, v98
	v_exp_f32_e32 v51, v99
	v_exp_f32_e32 v52, v100
	v_exp_f32_e32 v53, v101
	ds_read_b128 v[190:193], v3 offset:6144
	ds_read_b128 v[170:173], v3 offset:6656
	v_mfma_f32_32x32x16_bf16 v[34:49], v[178:181], v[12:15], v[34:49]
	v_exp_f32_e32 v54, v102
	v_exp_f32_e32 v55, v103
	v_exp_f32_e32 v56, v104
	v_exp_f32_e32 v57, v105
	ds_read_b128 v[178:181], v3 offset:8192
	ds_read_b128 v[166:169], v3 offset:8704
	v_mfma_f32_32x32x16_bf16 v[18:33], v[218:221], v[8:11], v[18:33]
	v_exp_f32_e32 v58, v106
	v_exp_f32_e32 v59, v107
	v_exp_f32_e32 v60, v108
	v_exp_f32_e32 v61, v109
	ds_read_b128 v[174:177], v3 offset:10240
	ds_read_b128 v[162:165], v3 offset:10752
	v_mfma_f32_32x32x16_bf16 v[34:49], v[218:221], v[4:7], v[34:49]
	v_exp_f32_e32 v62, v110
	v_exp_f32_e32 v63, v111
	v_exp_f32_e32 v64, v112
	v_exp_f32_e32 v65, v113
	s_mov_b32 s26, s27
	s_cmp_eq_u32 s27, s96
	s_cbranch_scc1 .Lmla_ss2_xdone
	s_add_i32 s64, s27, 3
	s_cmp_lt_u32 s64, s94
	s_cbranch_scc1 .Lmla_ss2_top
	s_branch .Lmla_ss_back
